# s12 variant: ALL PROJ epilogue stores write-through (sc1), not only the last unit
# speedup vs baseline: 1.0008x; 1.0008x over previous
; __device__ __forceinline__ unsigned cvt_pk_f16(float lo, float hi) { f32x2 v = {lo, hi}; h16x2 b = __builtin_convertvector(v, h16x2); return __builtin_bit_cast(unsigned, b); }
;     __device__ __forceinline__ void operator()(const f32x4 (&acc)[2][2][4][2], const Unit& u, int wr, int wc, int fr, int fq) const {
;         const int row0 = u.pm * BM + wr * 64 + fr, col0 = u.pn * BM + wc * 32 + 8 * fq;
; #pragma unroll
;         for (int ai = 0; ai < 2; ++ai)
; #pragma unroll
;             for (int m = 0; m < 4; ++m) { h16* rowp = C + (size_t)(row0 + ai * HALF + m * 16) * ldc + col0;
; #pragma unroll
;                 for (int bj = 0; bj < 2; ++bj) { const f32x4 v0 = acc[ai][bj][m][0], v1 = acc[ai][bj][m][1];
;                     u32x4 w; w.x = cvt_pk_f16(v0[0], v0[1]); w.y = cvt_pk_f16(v0[2], v0[3]); w.z = cvt_pk_f16(v1[0], v1[1]); w.w = cvt_pk_f16(v1[2], v1[3]);
;                     *(u32x4*)(rowp + bj * HALF) = w; } }
.LBB0_983:
	s_and_b64 vcc, exec, s[38:39]
	s_cbranch_vccz .Lproj_epi_last
	v_and_b32_e32 v224, -9, v140
	v_and_b32_e32 v225, 8, v140
	v_and_b32_e32 v226, 0x60, v142
	v_lshlrev_b32_e32 v225, 2, v225
	v_add3_u32 v226, v142, v226, v225
	v_lshl_add_u32 v150, s35, 8, v224
	v_lshl_or_b32 v144, s34, 8, v226
	v_ashrrev_i32_e32 v145, 31, v144
	v_mov_b64_e32 v[146:147], s[16:17]
	v_lshlrev_b64 v[144:145], 1, v[144:145]
	s_mov_b64 s[52:53], 0x1c000
	v_mad_i64_i32 v[152:153], s[34:35], v150, s91, v[146:147]
	v_lshl_add_u64 v[152:153], v[152:153], 0, v[144:145]
	v_add_u32_e32 v151, 0x10, v150
	v_mad_i64_i32 v[154:155], s[34:35], v151, s91, v[146:147]
	v_lshl_add_u64 v[154:155], v[154:155], 0, v[144:145]
	v_add_u32_e32 v151, 0x20, v150
	v_mad_i64_i32 v[156:157], s[34:35], v151, s91, v[146:147]
	v_lshl_add_u64 v[156:157], v[156:157], 0, v[144:145]
	v_add_u32_e32 v151, 0x30, v150
	v_mad_i64_i32 v[158:159], s[34:35], v151, s91, v[146:147]
	v_lshl_add_u64 v[158:159], v[158:159], 0, v[144:145]
	v_add_u32_e32 v151, 0x80, v150
	v_mad_i64_i32 v[160:161], s[34:35], v151, s91, v[146:147]
	v_lshl_add_u64 v[160:161], v[160:161], 0, v[144:145]
	v_add_u32_e32 v151, 0x90, v150
	v_mad_i64_i32 v[162:163], s[34:35], v151, s91, v[146:147]
	v_lshl_add_u64 v[162:163], v[162:163], 0, v[144:145]
	v_add_u32_e32 v151, 0xa0, v150
	v_mad_i64_i32 v[164:165], s[34:35], v151, s91, v[146:147]
	v_lshl_add_u64 v[164:165], v[164:165], 0, v[144:145]
	v_add_u32_e32 v151, 0xb0, v150
	v_mad_i64_i32 v[166:167], s[34:35], v151, s91, v[146:147]
	v_lshl_add_u64 v[166:167], v[166:167], 0, v[144:145]
	v_cvt_pk_f16_f32 v126, v126, v127
	v_cvt_pk_f16_f32 v127, v128, v129
	v_cvt_pk_f16_f32 v128, v122, v123
	v_cvt_pk_f16_f32 v129, v124, v125
	v_cvt_pk_f16_f32 v110, v110, v111
	v_cvt_pk_f16_f32 v111, v112, v113
	v_cvt_pk_f16_f32 v112, v106, v107
	v_cvt_pk_f16_f32 v113, v108, v109
	v_mov_b32_e32 v218, v110
	v_mov_b32_e32 v219, v111
	v_mov_b32_e32 v220, v112
	v_mov_b32_e32 v221, v113
	s_nop 1
	v_mov_b32_dpp v110, v126 row_ror:8 row_mask:0xf bank_mask:0x3
	v_mov_b32_dpp v111, v127 row_ror:8 row_mask:0xf bank_mask:0x3
	v_mov_b32_dpp v112, v128 row_ror:8 row_mask:0xf bank_mask:0x3
	v_mov_b32_dpp v113, v129 row_ror:8 row_mask:0xf bank_mask:0x3
	v_mov_b32_dpp v126, v218 row_ror:8 row_mask:0xf bank_mask:0xc
	v_mov_b32_dpp v127, v219 row_ror:8 row_mask:0xf bank_mask:0xc
	v_mov_b32_dpp v128, v220 row_ror:8 row_mask:0xf bank_mask:0xc
	v_mov_b32_dpp v129, v221 row_ror:8 row_mask:0xf bank_mask:0xc
	v_lshl_add_u64 v[168:169], v[152:153], 0, s[52:53]
	global_store_dwordx4 v[152:153], v[126:129], off sc1
	global_store_dwordx4 v[168:169], v[110:113], off sc1
	v_cvt_pk_f16_f32 v118, v118, v119
	v_cvt_pk_f16_f32 v119, v120, v121
	v_cvt_pk_f16_f32 v120, v114, v115
	v_cvt_pk_f16_f32 v121, v116, v117
	v_cvt_pk_f16_f32 v92, v92, v93
	v_cvt_pk_f16_f32 v93, v94, v95
	v_cvt_pk_f16_f32 v94, v88, v89
	v_cvt_pk_f16_f32 v95, v90, v91
	v_mov_b32_e32 v218, v92
	v_mov_b32_e32 v219, v93
	v_mov_b32_e32 v220, v94
	v_mov_b32_e32 v221, v95
	s_nop 1
	v_mov_b32_dpp v92, v118 row_ror:8 row_mask:0xf bank_mask:0x3
	v_mov_b32_dpp v93, v119 row_ror:8 row_mask:0xf bank_mask:0x3
	v_mov_b32_dpp v94, v120 row_ror:8 row_mask:0xf bank_mask:0x3
	v_mov_b32_dpp v95, v121 row_ror:8 row_mask:0xf bank_mask:0x3
	v_mov_b32_dpp v118, v218 row_ror:8 row_mask:0xf bank_mask:0xc
	v_mov_b32_dpp v119, v219 row_ror:8 row_mask:0xf bank_mask:0xc
	v_mov_b32_dpp v120, v220 row_ror:8 row_mask:0xf bank_mask:0xc
	v_mov_b32_dpp v121, v221 row_ror:8 row_mask:0xf bank_mask:0xc
	v_lshl_add_u64 v[168:169], v[154:155], 0, s[52:53]
	global_store_dwordx4 v[154:155], v[118:121], off sc1
	global_store_dwordx4 v[168:169], v[92:95], off sc1
	v_cvt_pk_f16_f32 v102, v102, v103
	v_cvt_pk_f16_f32 v103, v104, v105
	v_cvt_pk_f16_f32 v104, v98, v99
	v_cvt_pk_f16_f32 v105, v100, v101
	v_cvt_pk_f16_f32 v76, v76, v77
	v_cvt_pk_f16_f32 v77, v78, v79
	v_cvt_pk_f16_f32 v78, v72, v73
	v_cvt_pk_f16_f32 v79, v74, v75
	v_mov_b32_e32 v218, v76
	v_mov_b32_e32 v219, v77
	v_mov_b32_e32 v220, v78
	v_mov_b32_e32 v221, v79
	s_nop 1
	v_mov_b32_dpp v76, v102 row_ror:8 row_mask:0xf bank_mask:0x3
	v_mov_b32_dpp v77, v103 row_ror:8 row_mask:0xf bank_mask:0x3
	v_mov_b32_dpp v78, v104 row_ror:8 row_mask:0xf bank_mask:0x3
	v_mov_b32_dpp v79, v105 row_ror:8 row_mask:0xf bank_mask:0x3
	v_mov_b32_dpp v102, v218 row_ror:8 row_mask:0xf bank_mask:0xc
	v_mov_b32_dpp v103, v219 row_ror:8 row_mask:0xf bank_mask:0xc
	v_mov_b32_dpp v104, v220 row_ror:8 row_mask:0xf bank_mask:0xc
	v_mov_b32_dpp v105, v221 row_ror:8 row_mask:0xf bank_mask:0xc
	v_lshl_add_u64 v[168:169], v[156:157], 0, s[52:53]
	global_store_dwordx4 v[156:157], v[102:105], off sc1
	global_store_dwordx4 v[168:169], v[76:79], off sc1
	v_cvt_pk_f16_f32 v84, v84, v85
	v_cvt_pk_f16_f32 v85, v86, v87
	v_cvt_pk_f16_f32 v86, v80, v81
	v_cvt_pk_f16_f32 v87, v82, v83
	v_cvt_pk_f16_f32 v68, v68, v69
; __device__ __forceinline__ unsigned cvt_pk_f16(float lo, float hi) { f32x2 v = {lo, hi}; h16x2 b = __builtin_convertvector(v, h16x2); return __builtin_bit_cast(unsigned, b); }
;     __device__ __forceinline__ void operator()(const f32x4 (&acc)[2][2][4][2], const Unit& u, int wr, int wc, int fr, int fq) const {
;         const int row0 = u.pm * BM + wr * 64 + fr, col0 = u.pn * BM + wc * 32 + 8 * fq;
; #pragma unroll
;         for (int ai = 0; ai < 2; ++ai)
; #pragma unroll
;             for (int m = 0; m < 4; ++m) { h16* rowp = C + (size_t)(row0 + ai * HALF + m * 16) * ldc + col0;
; #pragma unroll
;                 for (int bj = 0; bj < 2; ++bj) { const f32x4 v0 = acc[ai][bj][m][0], v1 = acc[ai][bj][m][1];
;                     u32x4 w; w.x = cvt_pk_f16(v0[0], v0[1]); w.y = cvt_pk_f16(v0[2], v0[3]); w.z = cvt_pk_f16(v1[0], v1[1]); w.w = cvt_pk_f16(v1[2], v1[3]);
;                     *(u32x4*)(rowp + bj * HALF) = w; } }
	v_cvt_pk_f16_f32 v69, v70, v71
	v_cvt_pk_f16_f32 v70, v64, v65
	v_cvt_pk_f16_f32 v71, v66, v67
	v_mov_b32_e32 v218, v68
	v_mov_b32_e32 v219, v69
	v_mov_b32_e32 v220, v70
	v_mov_b32_e32 v221, v71
	s_nop 1
	v_mov_b32_dpp v68, v84 row_ror:8 row_mask:0xf bank_mask:0x3
	v_mov_b32_dpp v69, v85 row_ror:8 row_mask:0xf bank_mask:0x3
	v_mov_b32_dpp v70, v86 row_ror:8 row_mask:0xf bank_mask:0x3
	v_mov_b32_dpp v71, v87 row_ror:8 row_mask:0xf bank_mask:0x3
	v_mov_b32_dpp v84, v218 row_ror:8 row_mask:0xf bank_mask:0xc
	v_mov_b32_dpp v85, v219 row_ror:8 row_mask:0xf bank_mask:0xc
	v_mov_b32_dpp v86, v220 row_ror:8 row_mask:0xf bank_mask:0xc
	v_mov_b32_dpp v87, v221 row_ror:8 row_mask:0xf bank_mask:0xc
	v_lshl_add_u64 v[168:169], v[158:159], 0, s[52:53]
	global_store_dwordx4 v[158:159], v[84:87], off sc1
	global_store_dwordx4 v[168:169], v[68:71], off sc1
	v_cvt_pk_f16_f32 v60, v60, v61
	v_cvt_pk_f16_f32 v61, v62, v63
	v_cvt_pk_f16_f32 v62, v56, v57
	v_cvt_pk_f16_f32 v63, v58, v59
	v_cvt_pk_f16_f32 v44, v44, v45
	v_cvt_pk_f16_f32 v45, v46, v47
	v_cvt_pk_f16_f32 v46, v40, v41
	v_cvt_pk_f16_f32 v47, v42, v43
	v_mov_b32_e32 v218, v44
	v_mov_b32_e32 v219, v45
	v_mov_b32_e32 v220, v46
	v_mov_b32_e32 v221, v47
	s_nop 1
	v_mov_b32_dpp v44, v60 row_ror:8 row_mask:0xf bank_mask:0x3
	v_mov_b32_dpp v45, v61 row_ror:8 row_mask:0xf bank_mask:0x3
	v_mov_b32_dpp v46, v62 row_ror:8 row_mask:0xf bank_mask:0x3
	v_mov_b32_dpp v47, v63 row_ror:8 row_mask:0xf bank_mask:0x3
	v_mov_b32_dpp v60, v218 row_ror:8 row_mask:0xf bank_mask:0xc
	v_mov_b32_dpp v61, v219 row_ror:8 row_mask:0xf bank_mask:0xc
	v_mov_b32_dpp v62, v220 row_ror:8 row_mask:0xf bank_mask:0xc
	v_mov_b32_dpp v63, v221 row_ror:8 row_mask:0xf bank_mask:0xc
	v_lshl_add_u64 v[168:169], v[160:161], 0, s[52:53]
	global_store_dwordx4 v[160:161], v[60:63], off sc1
	global_store_dwordx4 v[168:169], v[44:47], off sc1
	v_cvt_pk_f16_f32 v52, v52, v53
	v_cvt_pk_f16_f32 v53, v54, v55
	v_cvt_pk_f16_f32 v54, v48, v49
	v_cvt_pk_f16_f32 v55, v50, v51
	v_cvt_pk_f16_f32 v28, v28, v29
	v_cvt_pk_f16_f32 v29, v30, v31
	v_cvt_pk_f16_f32 v30, v24, v25
	v_cvt_pk_f16_f32 v31, v26, v27
	v_mov_b32_e32 v218, v28
	v_mov_b32_e32 v219, v29
	v_mov_b32_e32 v220, v30
	v_mov_b32_e32 v221, v31
	s_nop 1
	v_mov_b32_dpp v28, v52 row_ror:8 row_mask:0xf bank_mask:0x3
	v_mov_b32_dpp v29, v53 row_ror:8 row_mask:0xf bank_mask:0x3
	v_mov_b32_dpp v30, v54 row_ror:8 row_mask:0xf bank_mask:0x3
	v_mov_b32_dpp v31, v55 row_ror:8 row_mask:0xf bank_mask:0x3
	v_mov_b32_dpp v52, v218 row_ror:8 row_mask:0xf bank_mask:0xc
	v_mov_b32_dpp v53, v219 row_ror:8 row_mask:0xf bank_mask:0xc
	v_mov_b32_dpp v54, v220 row_ror:8 row_mask:0xf bank_mask:0xc
	v_mov_b32_dpp v55, v221 row_ror:8 row_mask:0xf bank_mask:0xc
	v_lshl_add_u64 v[168:169], v[162:163], 0, s[52:53]
	global_store_dwordx4 v[162:163], v[52:55], off sc1
	global_store_dwordx4 v[168:169], v[28:31], off sc1
	v_cvt_pk_f16_f32 v36, v36, v37
	v_cvt_pk_f16_f32 v37, v38, v39
	v_cvt_pk_f16_f32 v38, v32, v33
	v_cvt_pk_f16_f32 v39, v34, v35
	v_cvt_pk_f16_f32 v12, v12, v13
	v_cvt_pk_f16_f32 v13, v14, v15
	v_cvt_pk_f16_f32 v14, v8, v9
	v_cvt_pk_f16_f32 v15, v10, v11
	v_mov_b32_e32 v218, v12
	v_mov_b32_e32 v219, v13
	v_mov_b32_e32 v220, v14
	v_mov_b32_e32 v221, v15
	s_nop 1
	v_mov_b32_dpp v12, v36 row_ror:8 row_mask:0xf bank_mask:0x3
	v_mov_b32_dpp v13, v37 row_ror:8 row_mask:0xf bank_mask:0x3
	v_mov_b32_dpp v14, v38 row_ror:8 row_mask:0xf bank_mask:0x3
	v_mov_b32_dpp v15, v39 row_ror:8 row_mask:0xf bank_mask:0x3
	v_mov_b32_dpp v36, v218 row_ror:8 row_mask:0xf bank_mask:0xc
	v_mov_b32_dpp v37, v219 row_ror:8 row_mask:0xf bank_mask:0xc
	v_mov_b32_dpp v38, v220 row_ror:8 row_mask:0xf bank_mask:0xc
	v_mov_b32_dpp v39, v221 row_ror:8 row_mask:0xf bank_mask:0xc
	v_lshl_add_u64 v[168:169], v[164:165], 0, s[52:53]
	global_store_dwordx4 v[164:165], v[36:39], off sc1
	global_store_dwordx4 v[168:169], v[12:15], off sc1
	v_cvt_pk_f16_f32 v20, v20, v21
	v_cvt_pk_f16_f32 v21, v22, v23
	v_cvt_pk_f16_f32 v22, v16, v17
	v_cvt_pk_f16_f32 v23, v18, v19
	v_cvt_pk_f16_f32 v4, v4, v5
	v_cvt_pk_f16_f32 v5, v6, v7
	v_cvt_pk_f16_f32 v6, v0, v1
	v_cvt_pk_f16_f32 v7, v2, v3
	v_mov_b32_e32 v218, v4
	v_mov_b32_e32 v219, v5
	v_mov_b32_e32 v220, v6
	v_mov_b32_e32 v221, v7
	s_nop 1
	v_mov_b32_dpp v4, v20 row_ror:8 row_mask:0xf bank_mask:0x3
	v_mov_b32_dpp v5, v21 row_ror:8 row_mask:0xf bank_mask:0x3
	v_mov_b32_dpp v6, v22 row_ror:8 row_mask:0xf bank_mask:0x3
	v_mov_b32_dpp v7, v23 row_ror:8 row_mask:0xf bank_mask:0x3
	v_mov_b32_dpp v20, v218 row_ror:8 row_mask:0xf bank_mask:0xc
	v_mov_b32_dpp v21, v219 row_ror:8 row_mask:0xf bank_mask:0xc
	v_mov_b32_dpp v22, v220 row_ror:8 row_mask:0xf bank_mask:0xc
	v_mov_b32_dpp v23, v221 row_ror:8 row_mask:0xf bank_mask:0xc
	v_lshl_add_u64 v[168:169], v[166:167], 0, s[52:53]
	global_store_dwordx4 v[166:167], v[20:23], off sc1
	global_store_dwordx4 v[168:169], v[4:7], off sc1
